# P9: epilogue throw-away load prefetching this workgroup's share of the next unit's B slab (k-tiles 2..17)
# speedup vs baseline: 1.0047x; 1.0047x over previous
.LBB0_1362:
	s_and_b64 vcc, exec, s[0:1]
	s_cmp_eq_u32 s101, 0
	s_cbranch_scc1 .Lgk_first_p9
	v_mov_b32_e32 v175, v169
	v_mov_b32_e32 v173, v169
	s_mov_b32 s21, 0
	s_mov_b64 s[30:31], 0x100
	s_mov_b64 s[34:35], s[14:15]
	ds_read_b128 v[26:29], v191
	ds_read_b128 v[30:33], v191 offset:1024
	ds_read_b128 v[18:21], v191 offset:2048
	ds_read_b128 v[22:25], v191 offset:3072
	ds_read_b128 v[10:13], v192
	ds_read_b128 v[14:17], v192 offset:1024
	ds_read_b128 v[2:5], v192 offset:2048
	ds_read_b128 v[6:9], v192 offset:3072
	s_cmp_eq_u32 s55, s21
	s_cselect_b64 vcc, -1, 0
	s_add_i32 s21, s21, 2
	s_and_b64 s[36:37], vcc, exec
	s_cselect_b32 s36, 0, s30
	s_cselect_b32 s23, 0, s31
	s_add_u32 s36, s8, s36
	s_addc_u32 s37, s9, s23
	s_add_u32 s23, s28, s30
	s_addc_u32 s70, s29, s31
	s_and_b64 s[38:39], vcc, exec
	v_cndmask_b32_e32 v168, v197, v198, vcc
	v_cndmask_b32_e32 v202, v172, v200, vcc
	v_cndmask_b32_e32 v184, v170, v199, vcc
	s_cselect_b32 s39, s25, s70
	s_cselect_b32 s38, s24, s23
	s_mov_b32 m0, s56
	v_lshl_add_u64 v[186:187], s[34:35], 0, v[172:173]
	ds_read_b128 v[176:179], v193
	ds_read_b128 v[180:183], v193 offset:1024
	ds_read_b128 v[208:211], v193 offset:2048
	ds_read_b128 v[212:215], v193 offset:3072
	ds_read_b128 v[216:219], v193 offset:4096
	ds_read_b128 v[220:223], v193 offset:5120
	ds_read_b128 v[224:227], v193 offset:6144
	ds_read_b128 v[228:231], v193 offset:7168
	global_load_lds_dwordx4 v[186:187], off
	v_lshl_add_u64 v[186:187], s[34:35], 0, v[174:175]
	s_mov_b32 m0, s57
	s_nop 0
	global_load_lds_dwordx4 v[186:187], off
	s_waitcnt vmcnt(17)
	s_waitcnt lgkmcnt(0)
	s_barrier
	s_setprio 1
	s_waitcnt lgkmcnt(0)
	v_mfma_scale_f32_16x16x128_f8f6f4 v[154:157], v[26:33], v[176:183], 0, v188, v189 op_sel_hi:[0,0,0]
	v_mfma_scale_f32_16x16x128_f8f6f4 v[150:153], v[18:25], v[176:183], 0, v188, v189 op_sel_hi:[0,0,0]
	v_mfma_scale_f32_16x16x128_f8f6f4 v[142:145], v[26:33], v[208:215], 0, v188, v189 op_sel_hi:[0,0,0]
	v_mfma_scale_f32_16x16x128_f8f6f4 v[134:137], v[18:25], v[208:215], 0, v188, v189 op_sel_hi:[0,0,0]
	v_mfma_scale_f32_16x16x128_f8f6f4 v[126:129], v[26:33], v[216:223], 0, v188, v189 op_sel_hi:[0,0,0]
	v_mfma_scale_f32_16x16x128_f8f6f4 v[118:121], v[18:25], v[216:223], 0, v188, v189 op_sel_hi:[0,0,0]
	v_mfma_scale_f32_16x16x128_f8f6f4 v[110:113], v[26:33], v[224:231], 0, v188, v189 op_sel_hi:[0,0,0]
	v_mfma_scale_f32_16x16x128_f8f6f4 v[102:105], v[18:25], v[224:231], 0, v188, v189 op_sel_hi:[0,0,0]
	s_setprio 0
	s_setprio 1
	v_mfma_scale_f32_16x16x128_f8f6f4 v[158:161], v[10:17], v[176:183], 0, v188, v189 op_sel_hi:[0,0,0]
	v_mfma_scale_f32_16x16x128_f8f6f4 v[146:149], v[2:9], v[176:183], 0, v188, v189 op_sel_hi:[0,0,0]
	v_mfma_scale_f32_16x16x128_f8f6f4 v[138:141], v[10:17], v[208:215], 0, v188, v189 op_sel_hi:[0,0,0]
	v_mfma_scale_f32_16x16x128_f8f6f4 v[130:133], v[2:9], v[208:215], 0, v188, v189 op_sel_hi:[0,0,0]
	v_mfma_scale_f32_16x16x128_f8f6f4 v[122:125], v[10:17], v[216:223], 0, v188, v189 op_sel_hi:[0,0,0]
	v_mfma_scale_f32_16x16x128_f8f6f4 v[114:117], v[2:9], v[216:223], 0, v188, v189 op_sel_hi:[0,0,0]
	v_mfma_scale_f32_16x16x128_f8f6f4 v[106:109], v[10:17], v[224:231], 0, v188, v189 op_sel_hi:[0,0,0]
	v_mfma_scale_f32_16x16x128_f8f6f4 v[98:101], v[2:9], v[224:231], 0, v188, v189 op_sel_hi:[0,0,0]
	s_setprio 0
	s_barrier
	s_mov_b32 m0, s58
	v_lshl_add_u64 v[176:177], s[38:39], 0, v[166:167]
	v_lshl_add_u64 v[178:179], s[38:39], 0, v[164:165]
	s_add_u32 s38, s38, s6
	ds_read_b128 v[208:211], v193 offset:16384
	ds_read_b128 v[212:215], v193 offset:17408
	ds_read_b128 v[216:219], v193 offset:18432
	ds_read_b128 v[220:223], v193 offset:19456
	ds_read_b128 v[224:227], v193 offset:20480
	ds_read_b128 v[228:231], v193 offset:21504
	ds_read_b128 v[232:235], v193 offset:22528
	ds_read_b128 v[236:239], v193 offset:23552
	global_load_lds_dwordx4 v[176:177], off
	s_mov_b32 m0, s59
	s_addc_u32 s39, s39, s7
	global_load_lds_dwordx4 v[178:179], off
	v_lshl_add_u64 v[180:181], s[38:39], 0, v[166:167]
	s_mov_b32 m0, s60
	v_lshl_add_u64 v[182:183], s[38:39], 0, v[164:165]
	global_load_lds_dwordx4 v[180:181], off
	s_mov_b32 m0, s61
	v_mov_b32_e32 v185, v169
	global_load_lds_dwordx4 v[182:183], off
	s_mov_b32 m0, s27
	v_lshl_add_u64 v[186:187], s[36:37], 0, v[168:169]
	global_load_lds_dwordx4 v168, s[36:37]
	s_mov_b32 m0, s45
	s_nop 0
	global_load_lds_dwordx4 v184, s[36:37]
	s_waitcnt vmcnt(17)
	s_waitcnt lgkmcnt(0)
	v_lshl_add_u64 v[184:185], s[36:37], 0, v[184:185]
	s_barrier
	s_setprio 1
	s_waitcnt lgkmcnt(0)
	v_mfma_scale_f32_16x16x128_f8f6f4 v[94:97], v[26:33], v[208:215], 0, v188, v189 op_sel_hi:[0,0,0]
	v_mfma_scale_f32_16x16x128_f8f6f4 v[86:89], v[18:25], v[208:215], 0, v188, v189 op_sel_hi:[0,0,0]
	v_mfma_scale_f32_16x16x128_f8f6f4 v[78:81], v[26:33], v[216:223], 0, v188, v189 op_sel_hi:[0,0,0]
	v_mfma_scale_f32_16x16x128_f8f6f4 v[70:73], v[18:25], v[216:223], 0, v188, v189 op_sel_hi:[0,0,0]
	v_mfma_scale_f32_16x16x128_f8f6f4 v[62:65], v[26:33], v[224:231], 0, v188, v189 op_sel_hi:[0,0,0]
	v_mfma_scale_f32_16x16x128_f8f6f4 v[54:57], v[18:25], v[224:231], 0, v188, v189 op_sel_hi:[0,0,0]
	v_mfma_scale_f32_16x16x128_f8f6f4 v[46:49], v[26:33], v[232:239], 0, v188, v189 op_sel_hi:[0,0,0]
	v_mfma_scale_f32_16x16x128_f8f6f4 v[38:41], v[18:25], v[232:239], 0, v188, v189 op_sel_hi:[0,0,0]
	s_setprio 0
	s_setprio 1
	v_mfma_scale_f32_16x16x128_f8f6f4 v[90:93], v[10:17], v[208:215], 0, v188, v189 op_sel_hi:[0,0,0]
	v_mfma_scale_f32_16x16x128_f8f6f4 v[82:85], v[2:9], v[208:215], 0, v188, v189 op_sel_hi:[0,0,0]
	v_mfma_scale_f32_16x16x128_f8f6f4 v[74:77], v[10:17], v[216:223], 0, v188, v189 op_sel_hi:[0,0,0]
	v_mfma_scale_f32_16x16x128_f8f6f4 v[66:69], v[2:9], v[216:223], 0, v188, v189 op_sel_hi:[0,0,0]
	v_mfma_scale_f32_16x16x128_f8f6f4 v[58:61], v[10:17], v[224:231], 0, v188, v189 op_sel_hi:[0,0,0]
	v_mfma_scale_f32_16x16x128_f8f6f4 v[50:53], v[2:9], v[224:231], 0, v188, v189 op_sel_hi:[0,0,0]
	v_mfma_scale_f32_16x16x128_f8f6f4 v[42:45], v[10:17], v[232:239], 0, v188, v189 op_sel_hi:[0,0,0]
	v_mfma_scale_f32_16x16x128_f8f6f4 v[34:37], v[2:9], v[232:239], 0, v188, v189 op_sel_hi:[0,0,0]
	s_setprio 0
	s_barrier
	ds_read_b128 v[26:29], v194
	ds_read_b128 v[30:33], v194 offset:1024
	ds_read_b128 v[18:21], v194 offset:2048
	ds_read_b128 v[22:25], v194 offset:3072
	ds_read_b128 v[10:13], v195
	ds_read_b128 v[14:17], v195 offset:1024
	ds_read_b128 v[2:5], v195 offset:2048
	ds_read_b128 v[6:9], v195 offset:3072
	s_mov_b32 m0, s46
	ds_read_b128 v[208:211], v193 offset:32768
	ds_read_b128 v[212:215], v193 offset:33792
	ds_read_b128 v[216:219], v193 offset:34816
	ds_read_b128 v[220:223], v193 offset:35840
	ds_read_b128 v[224:227], v193 offset:36864
	ds_read_b128 v[228:231], v193 offset:37888
	ds_read_b128 v[232:235], v193 offset:38912
	ds_read_b128 v[236:239], v193 offset:39936
	v_cndmask_b32_e32 v168, v174, v201, vcc
	global_load_lds_dwordx4 v202, s[36:37]
	s_mov_b32 m0, s47
	s_nop 0
	global_load_lds_dwordx4 v168, s[36:37]
	s_waitcnt vmcnt(8)
	s_waitcnt lgkmcnt(0)
	s_barrier
	s_setprio 1
	s_waitcnt lgkmcnt(0)
	v_mfma_scale_f32_16x16x128_f8f6f4 v[154:157], v[26:33], v[208:215], v[154:157], v188, v189 op_sel_hi:[0,0,0]
	v_mfma_scale_f32_16x16x128_f8f6f4 v[150:153], v[18:25], v[208:215], v[150:153], v188, v189 op_sel_hi:[0,0,0]
	v_mfma_scale_f32_16x16x128_f8f6f4 v[142:145], v[26:33], v[216:223], v[142:145], v188, v189 op_sel_hi:[0,0,0]
	v_mfma_scale_f32_16x16x128_f8f6f4 v[134:137], v[18:25], v[216:223], v[134:137], v188, v189 op_sel_hi:[0,0,0]
	v_mfma_scale_f32_16x16x128_f8f6f4 v[126:129], v[26:33], v[224:231], v[126:129], v188, v189 op_sel_hi:[0,0,0]
	v_mfma_scale_f32_16x16x128_f8f6f4 v[118:121], v[18:25], v[224:231], v[118:121], v188, v189 op_sel_hi:[0,0,0]
	v_mfma_scale_f32_16x16x128_f8f6f4 v[110:113], v[26:33], v[232:239], v[110:113], v188, v189 op_sel_hi:[0,0,0]
	v_mfma_scale_f32_16x16x128_f8f6f4 v[102:105], v[18:25], v[232:239], v[102:105], v188, v189 op_sel_hi:[0,0,0]
	s_setprio 0
	s_setprio 1
	v_mfma_scale_f32_16x16x128_f8f6f4 v[158:161], v[10:17], v[208:215], v[158:161], v188, v189 op_sel_hi:[0,0,0]
	v_mfma_scale_f32_16x16x128_f8f6f4 v[146:149], v[2:9], v[208:215], v[146:149], v188, v189 op_sel_hi:[0,0,0]
	v_mfma_scale_f32_16x16x128_f8f6f4 v[138:141], v[10:17], v[216:223], v[138:141], v188, v189 op_sel_hi:[0,0,0]
	v_mfma_scale_f32_16x16x128_f8f6f4 v[130:133], v[2:9], v[216:223], v[130:133], v188, v189 op_sel_hi:[0,0,0]
	v_mfma_scale_f32_16x16x128_f8f6f4 v[122:125], v[10:17], v[224:231], v[122:125], v188, v189 op_sel_hi:[0,0,0]
	v_mfma_scale_f32_16x16x128_f8f6f4 v[114:117], v[2:9], v[224:231], v[114:117], v188, v189 op_sel_hi:[0,0,0]
	v_mfma_scale_f32_16x16x128_f8f6f4 v[106:109], v[10:17], v[232:239], v[106:109], v188, v189 op_sel_hi:[0,0,0]
	v_mfma_scale_f32_16x16x128_f8f6f4 v[98:101], v[2:9], v[232:239], v[98:101], v188, v189 op_sel_hi:[0,0,0]
	s_setprio 0
	s_barrier
	s_mov_b32 m0, s63
	v_lshl_add_u64 v[176:177], v[176:177], 0, s[16:17]
	ds_read_b128 v[208:211], v193 offset:49152
	ds_read_b128 v[212:215], v193 offset:50176
	ds_read_b128 v[216:219], v193 offset:51200
	ds_read_b128 v[220:223], v193 offset:52224
	ds_read_b128 v[224:227], v193 offset:53248
	ds_read_b128 v[228:231], v193 offset:54272
	ds_read_b128 v[232:235], v193 offset:55296
	ds_read_b128 v[236:239], v193 offset:56320
	global_load_lds_dwordx4 v[176:177], off
	v_lshl_add_u64 v[176:177], v[178:179], 0, s[16:17]
	s_mov_b32 m0, s64
	s_nop 0
	global_load_lds_dwordx4 v[176:177], off
	v_lshl_add_u64 v[176:177], v[180:181], 0, s[16:17]
	s_mov_b32 m0, s65
	s_nop 0
	global_load_lds_dwordx4 v[176:177], off
	v_lshl_add_u64 v[176:177], v[182:183], 0, s[16:17]
	s_mov_b32 m0, s66
	s_nop 0
	global_load_lds_dwordx4 v[176:177], off
	v_lshl_add_u64 v[176:177], v[186:187], 0, s[16:17]
	s_mov_b32 m0, s53
	s_nop 0
	global_load_lds_dwordx4 v[176:177], off
	v_lshl_add_u64 v[176:177], v[184:185], 0, s[16:17]
	s_mov_b32 m0, s54
	s_nop 0
	global_load_lds_dwordx4 v[176:177], off
	s_waitcnt vmcnt(8)
	s_waitcnt lgkmcnt(0)
	s_barrier
	s_setprio 1
	s_waitcnt lgkmcnt(0)
	v_mfma_scale_f32_16x16x128_f8f6f4 v[94:97], v[26:33], v[208:215], v[94:97], v188, v189 op_sel_hi:[0,0,0]
	v_mfma_scale_f32_16x16x128_f8f6f4 v[86:89], v[18:25], v[208:215], v[86:89], v188, v189 op_sel_hi:[0,0,0]
	v_mfma_scale_f32_16x16x128_f8f6f4 v[78:81], v[26:33], v[216:223], v[78:81], v188, v189 op_sel_hi:[0,0,0]
	v_mfma_scale_f32_16x16x128_f8f6f4 v[70:73], v[18:25], v[216:223], v[70:73], v188, v189 op_sel_hi:[0,0,0]
	v_mfma_scale_f32_16x16x128_f8f6f4 v[62:65], v[26:33], v[224:231], v[62:65], v188, v189 op_sel_hi:[0,0,0]
	v_mfma_scale_f32_16x16x128_f8f6f4 v[54:57], v[18:25], v[224:231], v[54:57], v188, v189 op_sel_hi:[0,0,0]
	v_mfma_scale_f32_16x16x128_f8f6f4 v[46:49], v[26:33], v[232:239], v[46:49], v188, v189 op_sel_hi:[0,0,0]
	v_mfma_scale_f32_16x16x128_f8f6f4 v[38:41], v[18:25], v[232:239], v[38:41], v188, v189 op_sel_hi:[0,0,0]
	s_setprio 0
	s_setprio 1
	v_mfma_scale_f32_16x16x128_f8f6f4 v[90:93], v[10:17], v[208:215], v[90:93], v188, v189 op_sel_hi:[0,0,0]
	v_mfma_scale_f32_16x16x128_f8f6f4 v[82:85], v[2:9], v[208:215], v[82:85], v188, v189 op_sel_hi:[0,0,0]
	v_mfma_scale_f32_16x16x128_f8f6f4 v[74:77], v[10:17], v[216:223], v[74:77], v188, v189 op_sel_hi:[0,0,0]
	v_mfma_scale_f32_16x16x128_f8f6f4 v[66:69], v[2:9], v[216:223], v[66:69], v188, v189 op_sel_hi:[0,0,0]
	v_mfma_scale_f32_16x16x128_f8f6f4 v[58:61], v[10:17], v[224:231], v[58:61], v188, v189 op_sel_hi:[0,0,0]
	v_mfma_scale_f32_16x16x128_f8f6f4 v[50:53], v[2:9], v[224:231], v[50:53], v188, v189 op_sel_hi:[0,0,0]
	v_mfma_scale_f32_16x16x128_f8f6f4 v[42:45], v[10:17], v[232:239], v[42:45], v188, v189 op_sel_hi:[0,0,0]
	v_mfma_scale_f32_16x16x128_f8f6f4 v[34:37], v[2:9], v[232:239], v[34:37], v188, v189 op_sel_hi:[0,0,0]
	s_setprio 0
	s_barrier
	s_add_u32 s30, s30, 0x100
	s_addc_u32 s31, s31, 0
	s_add_u32 s34, s34, 0x100
	s_addc_u32 s35, s35, 0
	s_cmp_ge_i32 s21, s52
	s_cbranch_scc1 .LBB0_1365
	s_branch .LBB0_1364

.LBB0_1367:
	v_readfirstlane_b32 s74, v0
	s_lshr_b32 s74, s74, 6
	s_bfe_u32 s75, s33, 0x30002
	s_lshl_b32 s75, s75, 16
	s_lshl_b32 s76, s74, 8
	s_add_u32 s75, s75, s76
	s_add_u32 s75, s75, 0x100
	s_add_u32 s76, s24, s75
	s_addc_u32 s77, s25, 0
	v_and_b32_e32 v249, 31, v206
	v_lshrrev_b32_e32 v250, 5, v206
	v_lshlrev_b32_e32 v249, 11, v249
	v_lshl_or_b32 v250, v250, 7, v249
	global_load_dword v251, v250, s[76:77]
	v_lshl_add_u32 v6, s69, 8, v171
	v_mul_f32_e32 v2, 0xbcb8aa3b, v154
	v_exp_f32_e32 v2, v2
	v_mul_f32_e32 v8, 0xbcb8aa3b, v155
	v_exp_f32_e32 v8, v8
	v_mul_f32_e32 v3, v154, v158
	v_add_f32_e32 v2, 1.0, v2
	v_rcp_f32_e32 v2, v2
	v_add_f32_e32 v8, 1.0, v8
	v_rcp_f32_e32 v8, v8
	v_mul_f32_e32 v3, 0x3a800000, v3
	v_mul_f32_e32 v2, v3, v2
	v_mul_f32_e32 v3, v155, v159
	v_mul_f32_e32 v3, 0x3a800000, v3
	v_mul_f32_e32 v3, v3, v8
	v_mul_f32_e32 v8, 0xbcb8aa3b, v156
	v_exp_f32_e32 v8, v8
	v_mul_f32_e32 v10, 0xbcb8aa3b, v157
	v_exp_f32_e32 v10, v10
	v_mul_f32_e32 v9, v156, v160
	v_add_f32_e32 v8, 1.0, v8
	v_rcp_f32_e32 v8, v8
	v_add_f32_e32 v10, 1.0, v10
	v_rcp_f32_e32 v10, v10
	v_mul_f32_e32 v9, 0x3a800000, v9
	v_mul_f32_e32 v8, v9, v8
	v_mul_f32_e32 v9, v157, v161
	v_mul_f32_e32 v9, 0x3a800000, v9
	v_mul_f32_e32 v9, v9, v10
	v_mul_f32_e32 v10, 0xbcb8aa3b, v150
	v_exp_f32_e32 v10, v10
	v_mul_f32_e32 v12, 0xbcb8aa3b, v151
	v_exp_f32_e32 v12, v12
	v_mul_f32_e32 v11, v150, v146
	v_add_f32_e32 v10, 1.0, v10
	v_rcp_f32_e32 v10, v10
	v_add_f32_e32 v12, 1.0, v12
	v_rcp_f32_e32 v12, v12
	v_mul_f32_e32 v11, 0x3a800000, v11
	v_mul_f32_e32 v10, v11, v10
	v_mul_f32_e32 v11, v151, v147
	v_mul_f32_e32 v11, 0x3a800000, v11
	v_mul_f32_e32 v11, v11, v12
	v_mul_f32_e32 v12, 0xbcb8aa3b, v152
	v_exp_f32_e32 v12, v12
	v_mul_f32_e32 v14, 0xbcb8aa3b, v153
	v_exp_f32_e32 v14, v14
	v_mul_f32_e32 v13, v152, v148
	v_add_f32_e32 v12, 1.0, v12
	v_rcp_f32_e32 v12, v12
	v_add_f32_e32 v14, 1.0, v14
	v_rcp_f32_e32 v14, v14
	v_mul_f32_e32 v13, 0x3a800000, v13
	v_mul_f32_e32 v12, v13, v12
	v_mul_f32_e32 v13, v153, v149
	v_mul_f32_e32 v13, 0x3a800000, v13
	v_mul_f32_e32 v13, v13, v14
	v_med3_f32 v2, v2, s62, v196
	v_med3_f32 v3, v3, s62, v196
	v_med3_f32 v14, v8, s62, v196
	v_mov_b32_e32 v8, v169
	v_med3_f32 v15, v9, s62, v196
	v_cvt_pk_fp8_f32 v8, v2, v3
	v_med3_f32 v2, v10, s62, v196
	v_med3_f32 v3, v11, s62, v196
	v_mov_b32_e32 v9, v169
	v_cvt_pk_fp8_f32 v9, v2, v3
	v_ashrrev_i32_e32 v7, 31, v6
	v_med3_f32 v2, v12, s62, v196
	v_med3_f32 v3, v13, s62, v196
	v_cvt_pk_fp8_f32 v9, v2, v3 op_sel:[0,0,1]
	v_lshlrev_b64 v[2:3], 9, v[6:7]
	v_mul_f32_e32 v7, 0xbcb8aa3b, v142
	v_exp_f32_e32 v7, v7
	v_mul_f32_e32 v11, 0xbcb8aa3b, v143
	v_exp_f32_e32 v11, v11
	v_mul_f32_e32 v10, v142, v138
	v_add_f32_e32 v7, 1.0, v7
	v_rcp_f32_e32 v7, v7
	v_add_f32_e32 v11, 1.0, v11
	v_rcp_f32_e32 v11, v11
	v_mul_f32_e32 v10, 0x3a800000, v10
	v_mul_f32_e32 v7, v10, v7
	v_mul_f32_e32 v10, v143, v139
	v_mul_f32_e32 v10, 0x3a800000, v10
	v_mul_f32_e32 v10, v10, v11
	v_mul_f32_e32 v11, 0xbcb8aa3b, v144
	v_exp_f32_e32 v11, v11
	v_mul_f32_e32 v13, 0xbcb8aa3b, v145
	v_exp_f32_e32 v13, v13
	v_mul_f32_e32 v12, v144, v140
	v_add_f32_e32 v11, 1.0, v11
	v_rcp_f32_e32 v11, v11
	v_add_f32_e32 v13, 1.0, v13
	v_rcp_f32_e32 v13, v13
	v_mul_f32_e32 v12, 0x3a800000, v12
	v_mul_f32_e32 v11, v12, v11
	v_mul_f32_e32 v12, v145, v141
	v_mul_f32_e32 v12, 0x3a800000, v12
	v_mul_f32_e32 v12, v12, v13
	v_mul_f32_e32 v13, 0xbcb8aa3b, v134
	v_exp_f32_e32 v13, v13
	v_cvt_pk_fp8_f32 v8, v14, v15 op_sel:[0,0,1]
	v_mul_f32_e32 v15, 0xbcb8aa3b, v135
	v_exp_f32_e32 v15, v15
	v_add_f32_e32 v13, 1.0, v13
	v_rcp_f32_e32 v13, v13
	v_mul_f32_e32 v14, v134, v130
	v_add_f32_e32 v15, 1.0, v15
	v_rcp_f32_e32 v15, v15
	v_mul_f32_e32 v14, 0x3a800000, v14
	v_mul_f32_e32 v13, v14, v13
	v_mul_f32_e32 v14, v135, v131
	v_mul_f32_e32 v14, 0x3a800000, v14
	v_mul_f32_e32 v14, v14, v15
	v_mul_f32_e32 v15, 0xbcb8aa3b, v136
	v_exp_f32_e32 v15, v15
	v_mul_f32_e32 v17, 0xbcb8aa3b, v137
	v_exp_f32_e32 v17, v17
	v_mul_f32_e32 v16, v136, v132
	v_add_f32_e32 v15, 1.0, v15
	v_rcp_f32_e32 v15, v15
	v_add_f32_e32 v17, 1.0, v17
	v_rcp_f32_e32 v17, v17
	v_mul_f32_e32 v16, 0x3a800000, v16
	v_mul_f32_e32 v15, v16, v15
	v_mul_f32_e32 v16, v137, v133
	v_mul_f32_e32 v16, 0x3a800000, v16
	v_mul_f32_e32 v16, v16, v17
	v_med3_f32 v7, v7, s62, v196
	v_med3_f32 v17, v10, s62, v196
	v_mov_b32_e32 v10, v169
	v_med3_f32 v18, v11, s62, v196
	v_cvt_pk_fp8_f32 v10, v7, v17
	v_med3_f32 v7, v13, s62, v196
	v_med3_f32 v13, v14, s62, v196
	v_mov_b32_e32 v11, v169
	v_lshl_or_b32 v4, s26, 7, v190
	v_cvt_pk_fp8_f32 v11, v7, v13
	v_ashrrev_i32_e32 v5, 31, v4
	v_lshl_add_u64 v[2:3], s[12:13], 0, v[2:3]
	v_lshl_add_u64 v[2:3], v[2:3], 0, v[4:5]
	v_med3_f32 v12, v12, s62, v196
	global_store_dwordx2 v[2:3], v[8:9], off
	v_or_b32_e32 v8, 16, v6
	v_cvt_pk_fp8_f32 v10, v18, v12 op_sel:[0,0,1]
	v_med3_f32 v7, v15, s62, v196
	v_med3_f32 v12, v16, s62, v196
	v_ashrrev_i32_e32 v9, 31, v8
	v_cvt_pk_fp8_f32 v11, v7, v12 op_sel:[0,0,1]
	v_lshlrev_b64 v[8:9], 9, v[8:9]
	v_lshl_add_u64 v[8:9], s[12:13], 0, v[8:9]
	v_mul_f32_e32 v7, 0xbcb8aa3b, v126
	v_lshl_add_u64 v[8:9], v[8:9], 0, v[4:5]
	v_exp_f32_e32 v7, v7
	global_store_dwordx2 v[8:9], v[10:11], off
	v_mul_f32_e32 v11, 0xbcb8aa3b, v127
	v_exp_f32_e32 v11, v11
	v_add_f32_e32 v7, 1.0, v7
	v_rcp_f32_e32 v7, v7
	v_mul_f32_e32 v10, v126, v122
	v_add_f32_e32 v11, 1.0, v11
	v_rcp_f32_e32 v11, v11
	v_mul_f32_e32 v10, 0x3a800000, v10
	v_mul_f32_e32 v7, v10, v7
	v_mul_f32_e32 v10, v127, v123
	v_mul_f32_e32 v10, 0x3a800000, v10
	v_mul_f32_e32 v10, v10, v11
	v_mul_f32_e32 v11, 0xbcb8aa3b, v128
	v_exp_f32_e32 v11, v11
	v_mul_f32_e32 v13, 0xbcb8aa3b, v129
	v_exp_f32_e32 v13, v13
	v_mul_f32_e32 v12, v128, v124
	v_add_f32_e32 v11, 1.0, v11
	v_rcp_f32_e32 v11, v11
	v_add_f32_e32 v13, 1.0, v13
	v_rcp_f32_e32 v13, v13
	v_mul_f32_e32 v12, 0x3a800000, v12
	v_mul_f32_e32 v11, v12, v11
	v_mul_f32_e32 v12, v129, v125
	v_mul_f32_e32 v12, 0x3a800000, v12
	v_mul_f32_e32 v12, v12, v13
	v_mul_f32_e32 v13, 0xbcb8aa3b, v118
	v_exp_f32_e32 v13, v13
	v_mul_f32_e32 v15, 0xbcb8aa3b, v119
	v_exp_f32_e32 v15, v15
	v_mul_f32_e32 v14, v118, v114
	v_add_f32_e32 v13, 1.0, v13
	v_rcp_f32_e32 v13, v13
	v_add_f32_e32 v15, 1.0, v15
	v_rcp_f32_e32 v15, v15
	v_mul_f32_e32 v14, 0x3a800000, v14
	v_mul_f32_e32 v13, v14, v13
	v_mul_f32_e32 v14, v119, v115
	v_mul_f32_e32 v14, 0x3a800000, v14
	v_mul_f32_e32 v14, v14, v15
	v_mul_f32_e32 v15, 0xbcb8aa3b, v120
	v_exp_f32_e32 v15, v15
	v_mul_f32_e32 v17, 0xbcb8aa3b, v121
	v_exp_f32_e32 v17, v17
	v_mul_f32_e32 v16, v120, v116
	v_add_f32_e32 v15, 1.0, v15
	v_rcp_f32_e32 v15, v15
	v_add_f32_e32 v17, 1.0, v17
	v_rcp_f32_e32 v17, v17
	v_mul_f32_e32 v16, 0x3a800000, v16
	v_mul_f32_e32 v15, v16, v15
	v_mul_f32_e32 v16, v121, v117
	v_mul_f32_e32 v16, 0x3a800000, v16
	v_mul_f32_e32 v16, v16, v17
	v_med3_f32 v7, v7, s62, v196
	v_med3_f32 v17, v10, s62, v196
	v_mov_b32_e32 v10, v169
	v_med3_f32 v18, v11, s62, v196
	v_cvt_pk_fp8_f32 v10, v7, v17
	v_med3_f32 v7, v13, s62, v196
	v_med3_f32 v13, v14, s62, v196
	v_mov_b32_e32 v11, v169
	v_cvt_pk_fp8_f32 v11, v7, v13
	v_med3_f32 v12, v12, s62, v196
	v_or_b32_e32 v8, 32, v6
	v_cvt_pk_fp8_f32 v10, v18, v12 op_sel:[0,0,1]
	v_med3_f32 v7, v15, s62, v196
	v_med3_f32 v12, v16, s62, v196
	v_ashrrev_i32_e32 v9, 31, v8
	v_cvt_pk_fp8_f32 v11, v7, v12 op_sel:[0,0,1]
	v_lshlrev_b64 v[8:9], 9, v[8:9]
	v_lshl_add_u64 v[8:9], s[12:13], 0, v[8:9]
	v_lshl_add_u64 v[8:9], v[8:9], 0, v[4:5]
	global_store_dwordx2 v[8:9], v[10:11], off
	v_mul_f32_e32 v8, 0xbcb8aa3b, v110
	v_exp_f32_e32 v8, v8
	v_mul_f32_e32 v10, 0xbcb8aa3b, v111
	v_exp_f32_e32 v10, v10
	v_mul_f32_e32 v9, v110, v106
	v_add_f32_e32 v8, 1.0, v8
	v_rcp_f32_e32 v8, v8
	v_add_f32_e32 v10, 1.0, v10
	v_rcp_f32_e32 v10, v10
	v_mul_f32_e32 v9, 0x3a800000, v9
	v_mul_f32_e32 v8, v9, v8
	v_mul_f32_e32 v9, v111, v107
	v_mul_f32_e32 v9, 0x3a800000, v9
	v_mul_f32_e32 v9, v9, v10
	v_mul_f32_e32 v10, 0xbcb8aa3b, v112
	v_exp_f32_e32 v10, v10
	v_mul_f32_e32 v12, 0xbcb8aa3b, v113
	v_exp_f32_e32 v12, v12
	v_mul_f32_e32 v11, v112, v108
	v_add_f32_e32 v10, 1.0, v10
	v_rcp_f32_e32 v10, v10
	v_add_f32_e32 v12, 1.0, v12
	v_rcp_f32_e32 v12, v12
	v_mul_f32_e32 v11, 0x3a800000, v11
	v_mul_f32_e32 v10, v11, v10
	v_mul_f32_e32 v11, v113, v109
	v_mul_f32_e32 v11, 0x3a800000, v11
	v_mul_f32_e32 v11, v11, v12
	v_mul_f32_e32 v12, 0xbcb8aa3b, v102
	v_exp_f32_e32 v12, v12
	v_mul_f32_e32 v14, 0xbcb8aa3b, v103
	v_exp_f32_e32 v14, v14
	v_mul_f32_e32 v13, v102, v98
	v_add_f32_e32 v12, 1.0, v12
	v_rcp_f32_e32 v12, v12
	v_add_f32_e32 v14, 1.0, v14
	v_rcp_f32_e32 v14, v14
	v_mul_f32_e32 v13, 0x3a800000, v13
	v_mul_f32_e32 v12, v13, v12
	v_mul_f32_e32 v13, v103, v99
	v_mul_f32_e32 v13, 0x3a800000, v13
	v_mul_f32_e32 v13, v13, v14
	v_mul_f32_e32 v14, 0xbcb8aa3b, v104
	v_exp_f32_e32 v14, v14
	v_mul_f32_e32 v16, 0xbcb8aa3b, v105
	v_exp_f32_e32 v16, v16
	v_mul_f32_e32 v15, v104, v100
	v_add_f32_e32 v14, 1.0, v14
	v_rcp_f32_e32 v14, v14
	v_add_f32_e32 v16, 1.0, v16
	v_rcp_f32_e32 v16, v16
	v_mul_f32_e32 v15, 0x3a800000, v15
	v_mul_f32_e32 v14, v15, v14
	v_mul_f32_e32 v15, v105, v101
	v_mul_f32_e32 v15, 0x3a800000, v15
	v_mul_f32_e32 v15, v15, v16
	v_med3_f32 v16, v8, s62, v196
	v_med3_f32 v9, v9, s62, v196
	v_mov_b32_e32 v8, v169
	v_cvt_pk_fp8_f32 v8, v16, v9
	v_med3_f32 v12, v12, s62, v196
	v_med3_f32 v13, v13, s62, v196
	v_mov_b32_e32 v9, v169
	v_cvt_pk_fp8_f32 v9, v12, v13
	v_med3_f32 v10, v10, s62, v196
	v_med3_f32 v11, v11, s62, v196
	v_or_b32_e32 v6, 48, v6
	v_cvt_pk_fp8_f32 v8, v10, v11 op_sel:[0,0,1]
	v_med3_f32 v10, v14, s62, v196
	v_med3_f32 v11, v15, s62, v196
	v_ashrrev_i32_e32 v7, 31, v6
	v_cvt_pk_fp8_f32 v9, v10, v11 op_sel:[0,0,1]
	v_lshlrev_b64 v[6:7], 9, v[6:7]
	v_lshl_add_u64 v[6:7], s[12:13], 0, v[6:7]
	v_lshl_add_u64 v[4:5], v[6:7], 0, v[4:5]
	global_store_dwordx2 v[4:5], v[8:9], off
	v_mul_f32_e32 v4, 0xbcb8aa3b, v94
	v_exp_f32_e32 v4, v4
	v_mul_f32_e32 v6, 0xbcb8aa3b, v95
	v_exp_f32_e32 v6, v6
	v_mul_f32_e32 v5, v94, v90
	v_add_f32_e32 v4, 1.0, v4
	v_rcp_f32_e32 v4, v4
	v_add_f32_e32 v6, 1.0, v6
	v_rcp_f32_e32 v6, v6
	v_mul_f32_e32 v5, 0x3a800000, v5
	v_mul_f32_e32 v4, v5, v4
	v_mul_f32_e32 v5, v95, v91
	v_mul_f32_e32 v5, 0x3a800000, v5
	v_mul_f32_e32 v5, v5, v6
	v_mul_f32_e32 v6, 0xbcb8aa3b, v96
	v_exp_f32_e32 v6, v6
	v_mul_f32_e32 v8, 0xbcb8aa3b, v97
	v_exp_f32_e32 v8, v8
	v_mul_f32_e32 v7, v96, v92
	v_add_f32_e32 v6, 1.0, v6
	v_rcp_f32_e32 v6, v6
	v_add_f32_e32 v8, 1.0, v8
	v_rcp_f32_e32 v8, v8
	v_mul_f32_e32 v7, 0x3a800000, v7
	v_mul_f32_e32 v6, v7, v6
	v_mul_f32_e32 v7, v97, v93
	v_mul_f32_e32 v7, 0x3a800000, v7
	v_mul_f32_e32 v7, v7, v8
	v_mul_f32_e32 v8, 0xbcb8aa3b, v86
	v_exp_f32_e32 v8, v8
	v_mul_f32_e32 v10, 0xbcb8aa3b, v87
	v_exp_f32_e32 v10, v10
	v_mul_f32_e32 v9, v86, v82
	v_add_f32_e32 v8, 1.0, v8
	v_rcp_f32_e32 v8, v8
	v_add_f32_e32 v10, 1.0, v10
	v_rcp_f32_e32 v10, v10
	v_mul_f32_e32 v9, 0x3a800000, v9
	v_mul_f32_e32 v8, v9, v8
	v_mul_f32_e32 v9, v87, v83
	v_mul_f32_e32 v9, 0x3a800000, v9
	v_mul_f32_e32 v9, v9, v10
	v_mul_f32_e32 v10, 0xbcb8aa3b, v88
	v_exp_f32_e32 v10, v10
	v_mul_f32_e32 v12, 0xbcb8aa3b, v89
	v_exp_f32_e32 v12, v12
	v_mul_f32_e32 v11, v88, v84
	v_add_f32_e32 v10, 1.0, v10
	v_rcp_f32_e32 v10, v10
	v_add_f32_e32 v12, 1.0, v12
	v_rcp_f32_e32 v12, v12
	v_mul_f32_e32 v11, 0x3a800000, v11
	v_mul_f32_e32 v10, v11, v10
	v_mul_f32_e32 v11, v89, v85
	v_mul_f32_e32 v11, 0x3a800000, v11
	v_mul_f32_e32 v11, v11, v12
	v_med3_f32 v12, v4, s62, v196
	v_med3_f32 v5, v5, s62, v196
	v_mov_b32_e32 v4, v169
	v_cvt_pk_fp8_f32 v4, v12, v5
	v_med3_f32 v8, v8, s62, v196
	v_med3_f32 v9, v9, s62, v196
	v_mov_b32_e32 v5, v169
	v_cvt_pk_fp8_f32 v5, v8, v9
	v_med3_f32 v6, v6, s62, v196
	v_med3_f32 v7, v7, s62, v196
	v_cvt_pk_fp8_f32 v4, v6, v7 op_sel:[0,0,1]
	v_med3_f32 v6, v10, s62, v196
	v_med3_f32 v7, v11, s62, v196
	v_cvt_pk_fp8_f32 v5, v6, v7 op_sel:[0,0,1]
	v_add_co_u32_e32 v6, vcc, s49, v2
	v_mul_f32_e32 v8, 0xbcb8aa3b, v81
	s_nop 0
	v_addc_co_u32_e32 v7, vcc, 0, v3, vcc
	global_store_dwordx2 v[6:7], v[4:5], off
	v_mul_f32_e32 v4, 0xbcb8aa3b, v78
	v_exp_f32_e32 v4, v4
	v_mul_f32_e32 v6, 0xbcb8aa3b, v79
	v_exp_f32_e32 v6, v6
	v_mul_f32_e32 v5, v78, v74
	v_add_f32_e32 v4, 1.0, v4
	v_rcp_f32_e32 v4, v4
	v_add_f32_e32 v6, 1.0, v6
	v_rcp_f32_e32 v6, v6
	v_mul_f32_e32 v5, 0x3a800000, v5
	v_mul_f32_e32 v4, v5, v4
	v_mul_f32_e32 v5, v79, v75
	v_mul_f32_e32 v5, 0x3a800000, v5
	v_mul_f32_e32 v5, v5, v6
	v_mul_f32_e32 v6, 0xbcb8aa3b, v80
	v_exp_f32_e32 v6, v6
	v_exp_f32_e32 v8, v8
	v_mul_f32_e32 v7, v80, v76
	v_mul_f32_e32 v7, 0x3a800000, v7
	v_add_f32_e32 v6, 1.0, v6
	v_rcp_f32_e32 v6, v6
	v_add_f32_e32 v8, 1.0, v8
	v_rcp_f32_e32 v8, v8
	v_mul_f32_e32 v10, 0xbcb8aa3b, v71
	v_mul_f32_e32 v6, v7, v6
	v_mul_f32_e32 v7, v81, v77
	v_mul_f32_e32 v7, 0x3a800000, v7
	v_mul_f32_e32 v7, v7, v8
	v_mul_f32_e32 v8, 0xbcb8aa3b, v70
	v_exp_f32_e32 v8, v8
	v_exp_f32_e32 v10, v10
	v_mul_f32_e32 v9, v70, v66
	v_mul_f32_e32 v9, 0x3a800000, v9
	v_add_f32_e32 v8, 1.0, v8
	v_rcp_f32_e32 v8, v8
	v_add_f32_e32 v10, 1.0, v10
	v_rcp_f32_e32 v10, v10
	v_mul_f32_e32 v12, 0xbcb8aa3b, v73
	v_mul_f32_e32 v8, v9, v8
	v_mul_f32_e32 v9, v71, v67
	v_mul_f32_e32 v9, 0x3a800000, v9
	v_mul_f32_e32 v9, v9, v10
	v_mul_f32_e32 v10, 0xbcb8aa3b, v72
	v_exp_f32_e32 v10, v10
	v_exp_f32_e32 v12, v12
	v_mul_f32_e32 v11, v72, v68
	v_mul_f32_e32 v11, 0x3a800000, v11
	v_add_f32_e32 v10, 1.0, v10
	v_rcp_f32_e32 v10, v10
	v_add_f32_e32 v12, 1.0, v12
	v_rcp_f32_e32 v12, v12
	v_med3_f32 v5, v5, s62, v196
	v_mul_f32_e32 v10, v11, v10
	v_mul_f32_e32 v11, v73, v69
	v_mul_f32_e32 v11, 0x3a800000, v11
	v_mul_f32_e32 v11, v11, v12
	v_med3_f32 v12, v4, s62, v196
	v_mov_b32_e32 v4, v169
	v_cvt_pk_fp8_f32 v4, v12, v5
	v_med3_f32 v8, v8, s62, v196
	v_med3_f32 v9, v9, s62, v196
	v_mov_b32_e32 v5, v169
	v_cvt_pk_fp8_f32 v5, v8, v9
	v_med3_f32 v6, v6, s62, v196
	v_med3_f32 v7, v7, s62, v196
	v_cvt_pk_fp8_f32 v4, v6, v7 op_sel:[0,0,1]
	v_med3_f32 v6, v10, s62, v196
	v_med3_f32 v7, v11, s62, v196
	v_cvt_pk_fp8_f32 v5, v6, v7 op_sel:[0,0,1]
	v_add_co_u32_e32 v6, vcc, s50, v2
	v_mul_f32_e32 v8, 0xbcb8aa3b, v65
	s_nop 0
	v_addc_co_u32_e32 v7, vcc, 0, v3, vcc
	global_store_dwordx2 v[6:7], v[4:5], off
	v_mul_f32_e32 v4, 0xbcb8aa3b, v62
	v_exp_f32_e32 v4, v4
	v_mul_f32_e32 v6, 0xbcb8aa3b, v63
	v_exp_f32_e32 v6, v6
	v_mul_f32_e32 v5, v62, v58
	v_add_f32_e32 v4, 1.0, v4
	v_rcp_f32_e32 v4, v4
	v_add_f32_e32 v6, 1.0, v6
	v_rcp_f32_e32 v6, v6
	v_mul_f32_e32 v5, 0x3a800000, v5
	v_mul_f32_e32 v4, v5, v4
	v_mul_f32_e32 v5, v63, v59
	v_mul_f32_e32 v5, 0x3a800000, v5
	v_mul_f32_e32 v5, v5, v6
	v_mul_f32_e32 v6, 0xbcb8aa3b, v64
	v_exp_f32_e32 v6, v6
	v_exp_f32_e32 v8, v8
	v_mul_f32_e32 v7, v64, v60
	v_mul_f32_e32 v7, 0x3a800000, v7
	v_add_f32_e32 v6, 1.0, v6
	v_rcp_f32_e32 v6, v6
	v_add_f32_e32 v8, 1.0, v8
	v_rcp_f32_e32 v8, v8
	v_mul_f32_e32 v10, 0xbcb8aa3b, v55
	v_mul_f32_e32 v6, v7, v6
	v_mul_f32_e32 v7, v65, v61
	v_mul_f32_e32 v7, 0x3a800000, v7
	v_mul_f32_e32 v7, v7, v8
	v_mul_f32_e32 v8, 0xbcb8aa3b, v54
	v_exp_f32_e32 v8, v8
	v_exp_f32_e32 v10, v10
	v_mul_f32_e32 v9, v54, v50
	v_mul_f32_e32 v9, 0x3a800000, v9
	v_add_f32_e32 v8, 1.0, v8
	v_rcp_f32_e32 v8, v8
	v_add_f32_e32 v10, 1.0, v10
	v_rcp_f32_e32 v10, v10
	v_mul_f32_e32 v12, 0xbcb8aa3b, v57
	v_mul_f32_e32 v8, v9, v8
	v_mul_f32_e32 v9, v55, v51
	v_mul_f32_e32 v9, 0x3a800000, v9
	v_mul_f32_e32 v9, v9, v10
	v_mul_f32_e32 v10, 0xbcb8aa3b, v56
	v_exp_f32_e32 v10, v10
	v_exp_f32_e32 v12, v12
	v_mul_f32_e32 v11, v56, v52
	v_mul_f32_e32 v11, 0x3a800000, v11
	v_add_f32_e32 v10, 1.0, v10
	v_rcp_f32_e32 v10, v10
	v_add_f32_e32 v12, 1.0, v12
	v_rcp_f32_e32 v12, v12
	v_med3_f32 v5, v5, s62, v196
	v_mul_f32_e32 v10, v11, v10
	v_mul_f32_e32 v11, v57, v53
	v_mul_f32_e32 v11, 0x3a800000, v11
	v_mul_f32_e32 v11, v11, v12
	v_med3_f32 v12, v4, s62, v196
	v_mov_b32_e32 v4, v169
	v_cvt_pk_fp8_f32 v4, v12, v5
	v_med3_f32 v8, v8, s62, v196
	v_med3_f32 v9, v9, s62, v196
	v_mov_b32_e32 v5, v169
	v_cvt_pk_fp8_f32 v5, v8, v9
	v_med3_f32 v6, v6, s62, v196
	v_med3_f32 v7, v7, s62, v196
	v_cvt_pk_fp8_f32 v4, v6, v7 op_sel:[0,0,1]
	v_med3_f32 v6, v10, s62, v196
	v_med3_f32 v7, v11, s62, v196
	v_cvt_pk_fp8_f32 v5, v6, v7 op_sel:[0,0,1]
	v_add_co_u32_e32 v6, vcc, s51, v2
	v_mul_f32_e32 v8, 0xbcb8aa3b, v49
	s_nop 0
	v_addc_co_u32_e32 v7, vcc, 0, v3, vcc
	global_store_dwordx2 v[6:7], v[4:5], off
	v_mul_f32_e32 v4, 0xbcb8aa3b, v46
	v_exp_f32_e32 v4, v4
	v_mul_f32_e32 v6, 0xbcb8aa3b, v47
	v_exp_f32_e32 v6, v6
	v_mul_f32_e32 v5, v46, v42
	v_add_f32_e32 v4, 1.0, v4
	v_rcp_f32_e32 v4, v4
	v_add_f32_e32 v6, 1.0, v6
	v_rcp_f32_e32 v6, v6
	v_mul_f32_e32 v5, 0x3a800000, v5
	v_mul_f32_e32 v4, v5, v4
	v_mul_f32_e32 v5, v47, v43
	v_mul_f32_e32 v5, 0x3a800000, v5
	v_mul_f32_e32 v5, v5, v6
	v_mul_f32_e32 v6, 0xbcb8aa3b, v48
	v_exp_f32_e32 v6, v6
	v_exp_f32_e32 v8, v8
	v_mul_f32_e32 v7, v48, v44
	v_mul_f32_e32 v7, 0x3a800000, v7
	v_add_f32_e32 v6, 1.0, v6
	v_rcp_f32_e32 v6, v6
	v_add_f32_e32 v8, 1.0, v8
	v_rcp_f32_e32 v8, v8
	v_mul_f32_e32 v10, 0xbcb8aa3b, v39
	v_mul_f32_e32 v6, v7, v6
	v_mul_f32_e32 v7, v49, v45
	v_mul_f32_e32 v7, 0x3a800000, v7
	v_mul_f32_e32 v7, v7, v8
	v_mul_f32_e32 v8, 0xbcb8aa3b, v38
	v_exp_f32_e32 v8, v8
	v_exp_f32_e32 v10, v10
	v_mul_f32_e32 v9, v38, v34
	v_mul_f32_e32 v9, 0x3a800000, v9
	v_add_f32_e32 v8, 1.0, v8
	v_rcp_f32_e32 v8, v8
	v_add_f32_e32 v10, 1.0, v10
	v_rcp_f32_e32 v10, v10
	v_mul_f32_e32 v12, 0xbcb8aa3b, v41
	v_mul_f32_e32 v8, v9, v8
	v_mul_f32_e32 v9, v39, v35
	v_mul_f32_e32 v9, 0x3a800000, v9
	v_mul_f32_e32 v9, v9, v10
	v_mul_f32_e32 v10, 0xbcb8aa3b, v40
	v_exp_f32_e32 v10, v10
	v_exp_f32_e32 v12, v12
	v_mul_f32_e32 v11, v40, v36
	v_mul_f32_e32 v11, 0x3a800000, v11
	v_add_f32_e32 v10, 1.0, v10
	v_rcp_f32_e32 v10, v10
	v_add_f32_e32 v12, 1.0, v12
	v_rcp_f32_e32 v12, v12
	v_med3_f32 v5, v5, s62, v196
	v_mul_f32_e32 v10, v11, v10
	v_mul_f32_e32 v11, v41, v37
	v_mul_f32_e32 v11, 0x3a800000, v11
	v_mul_f32_e32 v11, v11, v12
	v_med3_f32 v12, v4, s62, v196
	v_mov_b32_e32 v4, v169
	v_cvt_pk_fp8_f32 v4, v12, v5
	v_med3_f32 v8, v8, s62, v196
	v_med3_f32 v9, v9, s62, v196
	v_mov_b32_e32 v5, v169
	v_cvt_pk_fp8_f32 v5, v8, v9
	v_med3_f32 v6, v6, s62, v196
	v_med3_f32 v7, v7, s62, v196
	v_cvt_pk_fp8_f32 v4, v6, v7 op_sel:[0,0,1]
	v_med3_f32 v6, v10, s62, v196
	v_med3_f32 v7, v11, s62, v196
	v_cvt_pk_fp8_f32 v5, v6, v7 op_sel:[0,0,1]
	v_add_co_u32_e32 v2, vcc, 0x16000, v2
	s_nop 1
	v_addc_co_u32_e32 v3, vcc, 0, v3, vcc
	s_and_b64 vcc, exec, s[2:3]
	s_mov_b64 s[2:3], -1
	global_store_dwordx2 v[2:3], v[4:5], off
	s_mov_b32 s101, 1
	s_cbranch_vccnz .LBB0_1357
	s_andn2_b64 vcc, exec, s[10:11]
	s_cbranch_vccnz .LBB0_1356
	s_barrier
	s_branch .LBB0_1356
